# GLA phase A state-tile section: the 16 LDS operand reads of its 8 MFMA groups issued up front into spare registers with counted waits (both code copies), on top of v72
# speedup vs baseline: 1.0066x; 1.0020x over previous
.LBB0_813:
	s_or_b64 exec, exec, s[84:85]
	s_waitcnt lgkmcnt(0)
	s_barrier
	ds_read_b128 v[0:3], v103 offset:32768
	ds_read_b128 v[4:7], v104 offset:50176
	ds_read_b128 v[8:11], v104 offset:51264
	s_waitcnt lgkmcnt(1)
	v_mfma_f32_16x16x32_bf16 v[4:7], v[4:7], v[0:3], 0
	s_lshl_b32 s76, s89, 5
	s_waitcnt lgkmcnt(0)
	v_mfma_f32_16x16x32_bf16 v[0:3], v[8:11], v[0:3], 0
	ds_read_b128 v[8:11], v103 offset:32832
	ds_read_b128 v[12:15], v104 offset:50240
	ds_read_b128 v[16:19], v104 offset:51328
	s_waitcnt lgkmcnt(1)
	v_mfma_f32_16x16x32_bf16 v[4:7], v[12:15], v[8:11], v[4:7]
	s_waitcnt lgkmcnt(0)
	v_mfma_f32_16x16x32_bf16 v[0:3], v[16:19], v[8:11], v[0:3]
	ds_read_b128 v[8:11], v103 offset:32896
	ds_read_b128 v[12:15], v104 offset:50304
	ds_read_b128 v[16:19], v104 offset:51392
	s_waitcnt lgkmcnt(1)
	v_mfma_f32_16x16x32_bf16 v[4:7], v[12:15], v[8:11], v[4:7]
	s_waitcnt lgkmcnt(0)
	v_mfma_f32_16x16x32_bf16 v[0:3], v[16:19], v[8:11], v[0:3]
	ds_read_b128 v[8:11], v103 offset:32960
	ds_read_b128 v[12:15], v104 offset:50368
	ds_read_b128 v[16:19], v104 offset:51456
	s_waitcnt lgkmcnt(1)
	v_mfma_f32_16x16x32_bf16 v[4:7], v[12:15], v[8:11], v[4:7]
	v_add_u32_e32 v14, 0, v94
	s_waitcnt lgkmcnt(0)
	v_mfma_f32_16x16x32_bf16 v[0:3], v[16:19], v[8:11], v[0:3]
	v_cndmask_b32_e64 v8, 0, 1, s[8:9]
	v_cndmask_b32_e64 v9, 0, 1, s[10:11]
	v_cndmask_b32_e64 v8, v9, v8, s[42:43]
	v_and_b32_e32 v8, 1, v8
	v_cmp_eq_u32_e32 vcc, 1, v8
	v_cndmask_b32_e64 v8, 0, 1, s[12:13]
	v_cndmask_b32_e64 v9, 0, 1, s[14:15]
	v_cndmask_b32_e64 v8, v9, v8, s[42:43]
	v_and_b32_e32 v8, 1, v8
	v_cndmask_b32_e32 v4, 0, v4, vcc
	v_cmp_eq_u32_e32 vcc, 1, v8
	v_cndmask_b32_e64 v8, 0, 1, s[16:17]
	v_cndmask_b32_e64 v9, 0, 1, s[18:19]
	v_cndmask_b32_e64 v8, v9, v8, s[42:43]
	v_and_b32_e32 v8, 1, v8
	v_cndmask_b32_e32 v5, 0, v5, vcc
	v_cmp_eq_u32_e32 vcc, 1, v8
	v_cndmask_b32_e64 v8, 0, 1, s[20:21]
	v_cndmask_b32_e64 v9, 0, 1, s[22:23]
	v_cndmask_b32_e64 v8, v9, v8, s[42:43]
	v_and_b32_e32 v8, 1, v8
	v_cndmask_b32_e32 v6, 0, v6, vcc
	v_cmp_eq_u32_e32 vcc, 1, v8
	v_cndmask_b32_e64 v8, 0, 1, s[24:25]
	v_cndmask_b32_e64 v9, 0, 1, s[26:27]
	v_cndmask_b32_e64 v8, v9, v8, s[42:43]
	v_and_b32_e32 v8, 1, v8
	v_cndmask_b32_e32 v7, 0, v7, vcc
	v_cmp_eq_u32_e32 vcc, 1, v8
	v_cndmask_b32_e64 v9, 0, 1, s[30:31]
	s_nop 0
	v_cndmask_b32_e32 v8, 0, v0, vcc
	v_cndmask_b32_e64 v0, 0, 1, s[28:29]
	v_cndmask_b32_e64 v0, v9, v0, s[42:43]
	v_and_b32_e32 v0, 1, v0
	v_cmp_eq_u32_e32 vcc, 1, v0
	v_cndmask_b32_e64 v0, 0, 1, s[34:35]
	s_nop 0
	v_cndmask_b32_e32 v9, 0, v1, vcc
	v_cndmask_b32_e64 v1, 0, 1, s[36:37]
	v_cndmask_b32_e64 v0, v1, v0, s[42:43]
	v_and_b32_e32 v0, 1, v0
	v_cmp_eq_u32_e32 vcc, 1, v0
	v_cndmask_b32_e64 v0, 0, 1, s[38:39]
	v_cndmask_b32_e64 v1, 0, 1, s[40:41]
	v_cndmask_b32_e64 v0, v1, v0, s[42:43]
	v_and_b32_e32 v0, 1, v0
	v_cndmask_b32_e32 v10, 0, v2, vcc
	v_cmp_eq_u32_e32 vcc, 1, v0
	v_cvt_pk_bf16_f32 v0, v4, v5
	v_cvt_pk_bf16_f32 v1, v6, v7
	v_cndmask_b32_e32 v3, 0, v3, vcc
	v_cvt_pk_bf16_f32 v2, v8, v9
	v_cvt_pk_bf16_f32 v3, v10, v3
	v_add_u32_e32 v4, s88, v94
	ds_write_b128 v4, v[0:3]
	v_add_u32_e32 v0, 0x15000, v14
	s_waitcnt lgkmcnt(0)
	s_barrier
	ds_read_b128 v[0:3], v0
	s_lshl_b64 s[82:83], s[82:83], 11
	v_lshlrev_b32_e32 v8, 5, v56
	v_mov_b32_e32 v9, v97
	v_lshl_add_u64 v[8:9], s[82:83], 0, v[8:9]
	v_add_u32_e32 v4, 0x16000, v14
	v_lshl_add_u64 v[10:11], v[70:71], 0, s[76:77]
	ds_read_b128 v[4:7], v4
	v_lshl_add_u64 v[12:13], v[10:11], 0, v[8:9]
	s_waitcnt lgkmcnt(1)
	v_mfma_f32_16x16x32_bf16 v[8:11], v[44:47], v[0:3], 0
	s_lshl_b64 s[42:43], s[92:93], 16
	s_add_i32 s92, s92, s96
	s_cmpk_lt_i32 s92, 0x480
	v_mfma_f32_16x16x32_bf16 v[0:3], v[36:39], v[0:3], 0
	s_waitcnt lgkmcnt(0)
	v_mfma_f32_16x16x32_bf16 v[0:3], v[32:35], v[4:7], v[0:3]
	v_mfma_f32_16x16x32_bf16 v[8:11], v[40:43], v[4:7], v[8:11]
	v_add_u32_e32 v4, 0x16400, v14
	s_nop 5
	v_cvt_pk_bf16_f32 v0, v0, v1
	v_cvt_pk_bf16_f32 v1, v2, v3
	global_store_dwordx2 v[12:13], v[0:1], off offset:512
	v_add_u32_e32 v0, 0x15400, v14
	ds_read_b128 v[0:3], v0
	ds_read_b128 v[4:7], v4
	v_cvt_pk_bf16_f32 v8, v8, v9
	v_cvt_pk_bf16_f32 v9, v10, v11
	global_store_dwordx2 v[12:13], v[8:9], off
	s_waitcnt lgkmcnt(1)
	v_mfma_f32_16x16x32_bf16 v[8:11], v[44:47], v[0:3], 0
	v_mfma_f32_16x16x32_bf16 v[0:3], v[36:39], v[0:3], 0
	s_waitcnt lgkmcnt(0)
	v_mfma_f32_16x16x32_bf16 v[8:11], v[40:43], v[4:7], v[8:11]
	v_mfma_f32_16x16x32_bf16 v[0:3], v[32:35], v[4:7], v[0:3]
	v_add_u32_e32 v4, 0x16800, v14
	s_nop 5
	v_cvt_pk_bf16_f32 v8, v8, v9
	v_cvt_pk_bf16_f32 v9, v10, v11
	v_add_co_u32_e32 v10, vcc, s65, v12
	ds_read_b128 v[4:7], v4
	s_nop 0
	v_addc_co_u32_e32 v11, vcc, 0, v13, vcc
	v_cvt_pk_bf16_f32 v0, v0, v1
	v_cvt_pk_bf16_f32 v1, v2, v3
	global_store_dwordx2 v[10:11], v[0:1], off offset:512
	v_add_u32_e32 v0, 0x15800, v14
	ds_read_b128 v[0:3], v0
	global_store_dwordx2 v[10:11], v[8:9], off
	s_waitcnt lgkmcnt(0)
	v_mfma_f32_16x16x32_bf16 v[8:11], v[44:47], v[0:3], 0
	v_mfma_f32_16x16x32_bf16 v[0:3], v[36:39], v[0:3], 0
	v_mfma_f32_16x16x32_bf16 v[8:11], v[40:43], v[4:7], v[8:11]
	v_mfma_f32_16x16x32_bf16 v[0:3], v[32:35], v[4:7], v[0:3]
	v_add_u32_e32 v4, 0x16c00, v14
	s_nop 5
	v_cvt_pk_bf16_f32 v8, v8, v9
	v_cvt_pk_bf16_f32 v9, v10, v11
	v_add_co_u32_e32 v10, vcc, s49, v12
	ds_read_b128 v[4:7], v4
	s_nop 0
	v_addc_co_u32_e32 v11, vcc, 0, v13, vcc
	v_cvt_pk_bf16_f32 v0, v0, v1
	v_cvt_pk_bf16_f32 v1, v2, v3
	global_store_dwordx2 v[10:11], v[0:1], off offset:512
	v_add_u32_e32 v0, 0x15c00, v14
	ds_read_b128 v[0:3], v0
	global_store_dwordx2 v[10:11], v[8:9], off
	s_waitcnt lgkmcnt(0)
	v_mfma_f32_16x16x32_bf16 v[8:11], v[44:47], v[0:3], 0
	v_mfma_f32_16x16x32_bf16 v[0:3], v[36:39], v[0:3], 0
	v_mfma_f32_16x16x32_bf16 v[8:11], v[40:43], v[4:7], v[8:11]
	v_mfma_f32_16x16x32_bf16 v[0:3], v[32:35], v[4:7], v[0:3]
	s_nop 6
	v_cvt_pk_bf16_f32 v8, v8, v9
	v_cvt_pk_bf16_f32 v9, v10, v11
	v_add_co_u32_e32 v10, vcc, s64, v12
	v_cvt_pk_bf16_f32 v0, v0, v1
	s_nop 0
	v_addc_co_u32_e32 v11, vcc, 0, v13, vcc
	v_cvt_pk_bf16_f32 v1, v2, v3
	global_store_dwordx2 v[10:11], v[8:9], off
	global_store_dwordx2 v[10:11], v[0:1], off offset:512
	ds_read_b128 v[136:139], v105
	ds_read_b128 v[140:143], v105 offset:64
	ds_read_b128 v[144:147], v105 offset:2304
	ds_read_b128 v[148:151], v105 offset:2368
	ds_read_b128 v[152:155], v105 offset:4608
	ds_read_b128 v[156:159], v105 offset:4672
	ds_read_b128 v[160:163], v105 offset:6912
	ds_read_b128 v[164:167], v105 offset:6976
	ds_read_b128 v[168:171], v105 offset:9216
	ds_read_b128 v[172:175], v105 offset:9280
	ds_read_b128 v[176:179], v105 offset:11520
	ds_read_b128 v[180:183], v105 offset:11584
	ds_read_b128 v[184:187], v105 offset:13824
	ds_read_b128 v[188:191], v105 offset:13888
	ds_read_b128 v[192:195], v105 offset:16128
	ds_read_b128 v[196:199], v105 offset:16192
	s_waitcnt lgkmcnt(15)
	v_mfma_f32_16x16x32_bf16 v[0:3], v[136:139], v[44:47], 0
	s_waitcnt lgkmcnt(15)
	v_mfma_f32_16x16x32_bf16 v[4:7], v[136:139], v[36:39], 0
	s_waitcnt lgkmcnt(14)
	v_mfma_f32_16x16x32_bf16 v[0:3], v[140:143], v[40:43], v[0:3]
	s_waitcnt lgkmcnt(14)
	v_mfma_f32_16x16x32_bf16 v[4:7], v[140:143], v[32:35], v[4:7]
	s_nop 6
	v_cvt_pk_bf16_f32 v12, v0, v1
	v_lshl_add_u64 v[0:1], s[42:43], 0, v[88:89]
	v_cvt_pk_bf16_f32 v13, v2, v3
	v_lshl_add_u64 v[2:3], v[72:73], 0, v[0:1]
	v_or_b32_e32 v0, 0x1000, v0
	v_cvt_pk_bf16_f32 v4, v4, v5
	v_cvt_pk_bf16_f32 v5, v6, v7
	v_lshl_add_u64 v[6:7], v[72:73], 0, v[0:1]
	global_store_dwordx2 v[2:3], v[12:13], off
	global_store_dwordx2 v[6:7], v[4:5], off
	s_waitcnt lgkmcnt(13)
	v_mfma_f32_16x16x32_bf16 v[12:15], v[144:147], v[44:47], 0
	s_waitcnt lgkmcnt(13)
	v_mfma_f32_16x16x32_bf16 v[4:7], v[144:147], v[36:39], 0
	s_waitcnt lgkmcnt(12)
	v_mfma_f32_16x16x32_bf16 v[12:15], v[148:151], v[40:43], v[12:15]
	s_waitcnt lgkmcnt(12)
	v_mfma_f32_16x16x32_bf16 v[4:7], v[148:151], v[32:35], v[4:7]
	s_nop 6
	v_cvt_pk_bf16_f32 v12, v12, v13
	v_cvt_pk_bf16_f32 v13, v14, v15
	v_cvt_pk_bf16_f32 v4, v4, v5
	v_cvt_pk_bf16_f32 v5, v6, v7
	v_lshl_add_u64 v[6:7], v[74:75], 0, v[0:1]
	global_store_dwordx2 v[2:3], v[12:13], off offset:512
	global_store_dwordx2 v[6:7], v[4:5], off
	s_waitcnt lgkmcnt(11)
	v_mfma_f32_16x16x32_bf16 v[12:15], v[152:155], v[44:47], 0
	s_waitcnt lgkmcnt(11)
	v_mfma_f32_16x16x32_bf16 v[4:7], v[152:155], v[36:39], 0
	s_waitcnt lgkmcnt(10)
	v_mfma_f32_16x16x32_bf16 v[12:15], v[156:159], v[40:43], v[12:15]
	s_waitcnt lgkmcnt(10)
	v_mfma_f32_16x16x32_bf16 v[4:7], v[156:159], v[32:35], v[4:7]
	s_nop 6
	v_cvt_pk_bf16_f32 v12, v12, v13
	v_cvt_pk_bf16_f32 v13, v14, v15
	v_cvt_pk_bf16_f32 v4, v4, v5
	v_cvt_pk_bf16_f32 v5, v6, v7
	v_lshl_add_u64 v[6:7], v[76:77], 0, v[0:1]
	global_store_dwordx2 v[2:3], v[12:13], off offset:1024
	global_store_dwordx2 v[6:7], v[4:5], off
	s_waitcnt lgkmcnt(9)
	v_mfma_f32_16x16x32_bf16 v[12:15], v[160:163], v[44:47], 0
	s_waitcnt lgkmcnt(9)
	v_mfma_f32_16x16x32_bf16 v[4:7], v[160:163], v[36:39], 0
	s_waitcnt lgkmcnt(8)
	v_mfma_f32_16x16x32_bf16 v[12:15], v[164:167], v[40:43], v[12:15]
	s_waitcnt lgkmcnt(8)
	v_mfma_f32_16x16x32_bf16 v[4:7], v[164:167], v[32:35], v[4:7]
	s_nop 6
	v_cvt_pk_bf16_f32 v12, v12, v13
	v_cvt_pk_bf16_f32 v13, v14, v15
	v_cvt_pk_bf16_f32 v4, v4, v5
	v_cvt_pk_bf16_f32 v5, v6, v7
	v_lshl_add_u64 v[6:7], v[78:79], 0, v[0:1]
	global_store_dwordx2 v[2:3], v[12:13], off offset:1536
	global_store_dwordx2 v[6:7], v[4:5], off
	s_waitcnt lgkmcnt(7)
	v_mfma_f32_16x16x32_bf16 v[12:15], v[168:171], v[44:47], 0
	s_waitcnt lgkmcnt(7)
	v_mfma_f32_16x16x32_bf16 v[4:7], v[168:171], v[36:39], 0
	s_waitcnt lgkmcnt(6)
	v_mfma_f32_16x16x32_bf16 v[12:15], v[172:175], v[40:43], v[12:15]
	s_waitcnt lgkmcnt(6)
	v_mfma_f32_16x16x32_bf16 v[4:7], v[172:175], v[32:35], v[4:7]
	s_nop 6
	v_cvt_pk_bf16_f32 v12, v12, v13
	v_cvt_pk_bf16_f32 v13, v14, v15
	v_cvt_pk_bf16_f32 v4, v4, v5
	v_cvt_pk_bf16_f32 v5, v6, v7
	v_lshl_add_u64 v[6:7], v[80:81], 0, v[0:1]
	global_store_dwordx2 v[2:3], v[12:13], off offset:2048
	global_store_dwordx2 v[6:7], v[4:5], off
	s_waitcnt lgkmcnt(5)
	v_mfma_f32_16x16x32_bf16 v[12:15], v[176:179], v[44:47], 0
	s_waitcnt lgkmcnt(5)
	v_mfma_f32_16x16x32_bf16 v[4:7], v[176:179], v[36:39], 0
	s_waitcnt lgkmcnt(4)
	v_mfma_f32_16x16x32_bf16 v[12:15], v[180:183], v[40:43], v[12:15]
	s_waitcnt lgkmcnt(4)
	v_mfma_f32_16x16x32_bf16 v[4:7], v[180:183], v[32:35], v[4:7]
	s_nop 6
	v_cvt_pk_bf16_f32 v12, v12, v13
	v_cvt_pk_bf16_f32 v13, v14, v15
	v_cvt_pk_bf16_f32 v4, v4, v5
	v_cvt_pk_bf16_f32 v5, v6, v7
	v_lshl_add_u64 v[6:7], v[82:83], 0, v[0:1]
	global_store_dwordx2 v[2:3], v[12:13], off offset:2560
	global_store_dwordx2 v[6:7], v[4:5], off
	s_waitcnt lgkmcnt(3)
	v_mfma_f32_16x16x32_bf16 v[12:15], v[184:187], v[44:47], 0
	s_waitcnt lgkmcnt(3)
	v_mfma_f32_16x16x32_bf16 v[4:7], v[184:187], v[36:39], 0
	s_waitcnt lgkmcnt(2)
	v_mfma_f32_16x16x32_bf16 v[12:15], v[188:191], v[40:43], v[12:15]
	s_waitcnt lgkmcnt(2)
	v_mfma_f32_16x16x32_bf16 v[4:7], v[188:191], v[32:35], v[4:7]
	s_nop 6
	v_cvt_pk_bf16_f32 v12, v12, v13
	v_cvt_pk_bf16_f32 v13, v14, v15
	v_cvt_pk_bf16_f32 v4, v4, v5
	v_cvt_pk_bf16_f32 v5, v6, v7
	v_lshl_add_u64 v[6:7], v[84:85], 0, v[0:1]
	global_store_dwordx2 v[2:3], v[12:13], off offset:3072
	global_store_dwordx2 v[6:7], v[4:5], off
	s_waitcnt lgkmcnt(1)
	v_mfma_f32_16x16x32_bf16 v[12:15], v[192:195], v[44:47], 0
	v_lshl_add_u64 v[0:1], v[86:87], 0, v[0:1]
	s_waitcnt lgkmcnt(0)
	v_mfma_f32_16x16x32_bf16 v[12:15], v[196:199], v[40:43], v[12:15]
	s_nop 7
	v_cvt_pk_bf16_f32 v12, v12, v13
	v_cvt_pk_bf16_f32 v13, v14, v15
	global_store_dwordx2 v[2:3], v[12:13], off offset:3584
	s_waitcnt lgkmcnt(1)
	v_mfma_f32_16x16x32_bf16 v[2:5], v[192:195], v[36:39], 0
	s_waitcnt lgkmcnt(0)
	v_mfma_f32_16x16x32_bf16 v[2:5], v[196:199], v[32:35], v[2:5]
	s_nop 7
	v_cvt_pk_bf16_f32 v2, v2, v3
	v_cvt_pk_bf16_f32 v3, v4, v5
	global_store_dwordx2 v[0:1], v[2:3], off
	s_cbranch_scc0 .LBB0_836

.LBB0_910:
	s_or_b64 exec, exec, s[86:87]
	s_waitcnt lgkmcnt(0)
	s_barrier
	ds_read_b128 v[0:3], v103 offset:32768
	ds_read_b128 v[4:7], v104 offset:50176
	ds_read_b128 v[8:11], v104 offset:51264
	s_waitcnt lgkmcnt(1)
	v_mfma_f32_16x16x32_bf16 v[4:7], v[4:7], v[0:3], 0
	s_lshl_b32 s76, s91, 5
	s_waitcnt lgkmcnt(0)
	v_mfma_f32_16x16x32_bf16 v[0:3], v[8:11], v[0:3], 0
	ds_read_b128 v[8:11], v103 offset:32832
	ds_read_b128 v[12:15], v104 offset:50240
	ds_read_b128 v[16:19], v104 offset:51328
	s_waitcnt lgkmcnt(1)
	v_mfma_f32_16x16x32_bf16 v[4:7], v[12:15], v[8:11], v[4:7]
	s_waitcnt lgkmcnt(0)
	v_mfma_f32_16x16x32_bf16 v[0:3], v[16:19], v[8:11], v[0:3]
	ds_read_b128 v[8:11], v103 offset:32896
	ds_read_b128 v[12:15], v104 offset:50304
	ds_read_b128 v[16:19], v104 offset:51392
	s_waitcnt lgkmcnt(1)
	v_mfma_f32_16x16x32_bf16 v[4:7], v[12:15], v[8:11], v[4:7]
	s_waitcnt lgkmcnt(0)
	v_mfma_f32_16x16x32_bf16 v[0:3], v[16:19], v[8:11], v[0:3]
	ds_read_b128 v[8:11], v103 offset:32960
	ds_read_b128 v[12:15], v104 offset:50368
	ds_read_b128 v[16:19], v104 offset:51456
	s_waitcnt lgkmcnt(1)
	v_mfma_f32_16x16x32_bf16 v[4:7], v[12:15], v[8:11], v[4:7]
	v_add_u32_e32 v14, 0, v94
	s_waitcnt lgkmcnt(0)
	v_mfma_f32_16x16x32_bf16 v[0:3], v[16:19], v[8:11], v[0:3]
	v_cndmask_b32_e64 v8, 0, 1, s[8:9]
	v_cndmask_b32_e64 v9, 0, 1, s[10:11]
	v_cndmask_b32_e64 v8, v9, v8, s[42:43]
	v_and_b32_e32 v8, 1, v8
	v_cmp_eq_u32_e32 vcc, 1, v8
	v_cndmask_b32_e64 v8, 0, 1, s[12:13]
	v_cndmask_b32_e64 v9, 0, 1, s[14:15]
	v_cndmask_b32_e64 v8, v9, v8, s[42:43]
	v_and_b32_e32 v8, 1, v8
	v_cndmask_b32_e32 v4, 0, v4, vcc
	v_cmp_eq_u32_e32 vcc, 1, v8
	v_cndmask_b32_e64 v8, 0, 1, s[16:17]
	v_cndmask_b32_e64 v9, 0, 1, s[18:19]
	v_cndmask_b32_e64 v8, v9, v8, s[42:43]
	v_and_b32_e32 v8, 1, v8
	v_cndmask_b32_e32 v5, 0, v5, vcc
	v_cmp_eq_u32_e32 vcc, 1, v8
	v_cndmask_b32_e64 v8, 0, 1, s[20:21]
	v_cndmask_b32_e64 v9, 0, 1, s[22:23]
	v_cndmask_b32_e64 v8, v9, v8, s[42:43]
	v_and_b32_e32 v8, 1, v8
	v_cndmask_b32_e32 v6, 0, v6, vcc
	v_cmp_eq_u32_e32 vcc, 1, v8
	v_cndmask_b32_e64 v8, 0, 1, s[24:25]
	v_cndmask_b32_e64 v9, 0, 1, s[26:27]
	v_cndmask_b32_e64 v8, v9, v8, s[42:43]
	v_and_b32_e32 v8, 1, v8
	v_cndmask_b32_e32 v7, 0, v7, vcc
	v_cmp_eq_u32_e32 vcc, 1, v8
	v_cndmask_b32_e64 v9, 0, 1, s[30:31]
	s_nop 0
	v_cndmask_b32_e32 v8, 0, v0, vcc
	v_cndmask_b32_e64 v0, 0, 1, s[28:29]
	v_cndmask_b32_e64 v0, v9, v0, s[42:43]
	v_and_b32_e32 v0, 1, v0
	v_cmp_eq_u32_e32 vcc, 1, v0
	v_cndmask_b32_e64 v0, 0, 1, s[34:35]
	s_nop 0
	v_cndmask_b32_e32 v9, 0, v1, vcc
	v_cndmask_b32_e64 v1, 0, 1, s[36:37]
	v_cndmask_b32_e64 v0, v1, v0, s[42:43]
	v_and_b32_e32 v0, 1, v0
	v_cmp_eq_u32_e32 vcc, 1, v0
	v_cndmask_b32_e64 v0, 0, 1, s[38:39]
	v_cndmask_b32_e64 v1, 0, 1, s[40:41]
	v_cndmask_b32_e64 v0, v1, v0, s[42:43]
	v_and_b32_e32 v0, 1, v0
	v_cndmask_b32_e32 v10, 0, v2, vcc
	v_cmp_eq_u32_e32 vcc, 1, v0
	v_cvt_pk_bf16_f32 v0, v4, v5
	v_cvt_pk_bf16_f32 v1, v6, v7
	v_cndmask_b32_e32 v3, 0, v3, vcc
	v_cvt_pk_bf16_f32 v2, v8, v9
	v_cvt_pk_bf16_f32 v3, v10, v3
	v_add_u32_e32 v4, s90, v94
	ds_write_b128 v4, v[0:3]
	v_add_u32_e32 v0, 0x15000, v14
	s_waitcnt lgkmcnt(0)
	s_barrier
	ds_read_b128 v[0:3], v0
	s_lshl_b64 s[84:85], s[84:85], 11
	v_lshlrev_b32_e32 v8, 5, v56
	v_mov_b32_e32 v9, v97
	v_lshl_add_u64 v[8:9], s[84:85], 0, v[8:9]
	v_add_u32_e32 v4, 0x16000, v14
	v_lshl_add_u64 v[10:11], v[70:71], 0, s[76:77]
	ds_read_b128 v[4:7], v4
	v_lshl_add_u64 v[12:13], v[10:11], 0, v[8:9]
	s_waitcnt lgkmcnt(1)
	v_mfma_f32_16x16x32_bf16 v[8:11], v[44:47], v[0:3], 0
	s_lshl_b64 s[42:43], s[78:79], 16
	s_add_i32 s78, s78, s96
	s_cmpk_lt_i32 s78, 0x480
	v_mfma_f32_16x16x32_bf16 v[0:3], v[36:39], v[0:3], 0
	s_waitcnt lgkmcnt(0)
	v_mfma_f32_16x16x32_bf16 v[0:3], v[32:35], v[4:7], v[0:3]
	v_mfma_f32_16x16x32_bf16 v[8:11], v[40:43], v[4:7], v[8:11]
	v_add_u32_e32 v4, 0x16400, v14
	s_nop 5
	v_cvt_pk_bf16_f32 v0, v0, v1
	v_cvt_pk_bf16_f32 v1, v2, v3
	global_store_dwordx2 v[12:13], v[0:1], off offset:512
	v_add_u32_e32 v0, 0x15400, v14
	ds_read_b128 v[0:3], v0
	ds_read_b128 v[4:7], v4
	v_cvt_pk_bf16_f32 v8, v8, v9
	v_cvt_pk_bf16_f32 v9, v10, v11
	global_store_dwordx2 v[12:13], v[8:9], off
	s_waitcnt lgkmcnt(1)
	v_mfma_f32_16x16x32_bf16 v[8:11], v[44:47], v[0:3], 0
	v_mfma_f32_16x16x32_bf16 v[0:3], v[36:39], v[0:3], 0
	s_waitcnt lgkmcnt(0)
	v_mfma_f32_16x16x32_bf16 v[8:11], v[40:43], v[4:7], v[8:11]
	v_mfma_f32_16x16x32_bf16 v[0:3], v[32:35], v[4:7], v[0:3]
	v_add_u32_e32 v4, 0x16800, v14
	s_nop 5
	v_cvt_pk_bf16_f32 v8, v8, v9
	v_cvt_pk_bf16_f32 v9, v10, v11
	v_add_co_u32_e32 v10, vcc, s65, v12
	ds_read_b128 v[4:7], v4
	s_nop 0
	v_addc_co_u32_e32 v11, vcc, 0, v13, vcc
	v_cvt_pk_bf16_f32 v0, v0, v1
	v_cvt_pk_bf16_f32 v1, v2, v3
	global_store_dwordx2 v[10:11], v[0:1], off offset:512
	v_add_u32_e32 v0, 0x15800, v14
	ds_read_b128 v[0:3], v0
	global_store_dwordx2 v[10:11], v[8:9], off
	s_waitcnt lgkmcnt(0)
	v_mfma_f32_16x16x32_bf16 v[8:11], v[44:47], v[0:3], 0
	v_mfma_f32_16x16x32_bf16 v[0:3], v[36:39], v[0:3], 0
	v_mfma_f32_16x16x32_bf16 v[8:11], v[40:43], v[4:7], v[8:11]
	v_mfma_f32_16x16x32_bf16 v[0:3], v[32:35], v[4:7], v[0:3]
	v_add_u32_e32 v4, 0x16c00, v14
	s_nop 5
	v_cvt_pk_bf16_f32 v8, v8, v9
	v_cvt_pk_bf16_f32 v9, v10, v11
	v_add_co_u32_e32 v10, vcc, s49, v12
	ds_read_b128 v[4:7], v4
	s_nop 0
	v_addc_co_u32_e32 v11, vcc, 0, v13, vcc
	v_cvt_pk_bf16_f32 v0, v0, v1
	v_cvt_pk_bf16_f32 v1, v2, v3
	global_store_dwordx2 v[10:11], v[0:1], off offset:512
	v_add_u32_e32 v0, 0x15c00, v14
	ds_read_b128 v[0:3], v0
	global_store_dwordx2 v[10:11], v[8:9], off
	s_waitcnt lgkmcnt(0)
	v_mfma_f32_16x16x32_bf16 v[8:11], v[44:47], v[0:3], 0
	v_mfma_f32_16x16x32_bf16 v[0:3], v[36:39], v[0:3], 0
	v_mfma_f32_16x16x32_bf16 v[8:11], v[40:43], v[4:7], v[8:11]
	v_mfma_f32_16x16x32_bf16 v[0:3], v[32:35], v[4:7], v[0:3]
	s_nop 6
	v_cvt_pk_bf16_f32 v8, v8, v9
	v_cvt_pk_bf16_f32 v9, v10, v11
	v_add_co_u32_e32 v10, vcc, s64, v12
	v_cvt_pk_bf16_f32 v0, v0, v1
	s_nop 0
	v_addc_co_u32_e32 v11, vcc, 0, v13, vcc
	v_cvt_pk_bf16_f32 v1, v2, v3
	global_store_dwordx2 v[10:11], v[8:9], off
	global_store_dwordx2 v[10:11], v[0:1], off offset:512
	ds_read_b128 v[136:139], v105
	ds_read_b128 v[140:143], v105 offset:64
	ds_read_b128 v[144:147], v105 offset:2304
	ds_read_b128 v[148:151], v105 offset:2368
	ds_read_b128 v[152:155], v105 offset:4608
	ds_read_b128 v[156:159], v105 offset:4672
	ds_read_b128 v[160:163], v105 offset:6912
	ds_read_b128 v[164:167], v105 offset:6976
	ds_read_b128 v[168:171], v105 offset:9216
	ds_read_b128 v[172:175], v105 offset:9280
	ds_read_b128 v[176:179], v105 offset:11520
	ds_read_b128 v[180:183], v105 offset:11584
	ds_read_b128 v[184:187], v105 offset:13824
	ds_read_b128 v[188:191], v105 offset:13888
	ds_read_b128 v[192:195], v105 offset:16128
	ds_read_b128 v[196:199], v105 offset:16192
	s_waitcnt lgkmcnt(15)
	v_mfma_f32_16x16x32_bf16 v[0:3], v[136:139], v[44:47], 0
	s_waitcnt lgkmcnt(15)
	v_mfma_f32_16x16x32_bf16 v[4:7], v[136:139], v[36:39], 0
	s_waitcnt lgkmcnt(14)
	v_mfma_f32_16x16x32_bf16 v[0:3], v[140:143], v[40:43], v[0:3]
	s_waitcnt lgkmcnt(14)
	v_mfma_f32_16x16x32_bf16 v[4:7], v[140:143], v[32:35], v[4:7]
	s_nop 6
	v_cvt_pk_bf16_f32 v12, v0, v1
	v_lshl_add_u64 v[0:1], s[42:43], 0, v[88:89]
	v_cvt_pk_bf16_f32 v13, v2, v3
	v_lshl_add_u64 v[2:3], v[72:73], 0, v[0:1]
	v_or_b32_e32 v0, 0x1000, v0
	v_cvt_pk_bf16_f32 v4, v4, v5
	v_cvt_pk_bf16_f32 v5, v6, v7
	v_lshl_add_u64 v[6:7], v[72:73], 0, v[0:1]
	global_store_dwordx2 v[2:3], v[12:13], off
	global_store_dwordx2 v[6:7], v[4:5], off
	s_waitcnt lgkmcnt(13)
	v_mfma_f32_16x16x32_bf16 v[12:15], v[144:147], v[44:47], 0
	s_waitcnt lgkmcnt(13)
	v_mfma_f32_16x16x32_bf16 v[4:7], v[144:147], v[36:39], 0
	s_waitcnt lgkmcnt(12)
	v_mfma_f32_16x16x32_bf16 v[12:15], v[148:151], v[40:43], v[12:15]
	s_waitcnt lgkmcnt(12)
	v_mfma_f32_16x16x32_bf16 v[4:7], v[148:151], v[32:35], v[4:7]
	s_nop 6
	v_cvt_pk_bf16_f32 v12, v12, v13
	v_cvt_pk_bf16_f32 v13, v14, v15
	v_cvt_pk_bf16_f32 v4, v4, v5
	v_cvt_pk_bf16_f32 v5, v6, v7
	v_lshl_add_u64 v[6:7], v[74:75], 0, v[0:1]
	global_store_dwordx2 v[2:3], v[12:13], off offset:512
	global_store_dwordx2 v[6:7], v[4:5], off
	s_waitcnt lgkmcnt(11)
	v_mfma_f32_16x16x32_bf16 v[12:15], v[152:155], v[44:47], 0
	s_waitcnt lgkmcnt(11)
	v_mfma_f32_16x16x32_bf16 v[4:7], v[152:155], v[36:39], 0
	s_waitcnt lgkmcnt(10)
	v_mfma_f32_16x16x32_bf16 v[12:15], v[156:159], v[40:43], v[12:15]
	s_waitcnt lgkmcnt(10)
	v_mfma_f32_16x16x32_bf16 v[4:7], v[156:159], v[32:35], v[4:7]
	s_nop 6
	v_cvt_pk_bf16_f32 v12, v12, v13
	v_cvt_pk_bf16_f32 v13, v14, v15
	v_cvt_pk_bf16_f32 v4, v4, v5
	v_cvt_pk_bf16_f32 v5, v6, v7
	v_lshl_add_u64 v[6:7], v[76:77], 0, v[0:1]
	global_store_dwordx2 v[2:3], v[12:13], off offset:1024
	global_store_dwordx2 v[6:7], v[4:5], off
	s_waitcnt lgkmcnt(9)
	v_mfma_f32_16x16x32_bf16 v[12:15], v[160:163], v[44:47], 0
	s_waitcnt lgkmcnt(9)
	v_mfma_f32_16x16x32_bf16 v[4:7], v[160:163], v[36:39], 0
	s_waitcnt lgkmcnt(8)
	v_mfma_f32_16x16x32_bf16 v[12:15], v[164:167], v[40:43], v[12:15]
	s_waitcnt lgkmcnt(8)
	v_mfma_f32_16x16x32_bf16 v[4:7], v[164:167], v[32:35], v[4:7]
	s_nop 6
	v_cvt_pk_bf16_f32 v12, v12, v13
	v_cvt_pk_bf16_f32 v13, v14, v15
	v_cvt_pk_bf16_f32 v4, v4, v5
	v_cvt_pk_bf16_f32 v5, v6, v7
	v_lshl_add_u64 v[6:7], v[78:79], 0, v[0:1]
	global_store_dwordx2 v[2:3], v[12:13], off offset:1536
	global_store_dwordx2 v[6:7], v[4:5], off
	s_waitcnt lgkmcnt(7)
	v_mfma_f32_16x16x32_bf16 v[12:15], v[168:171], v[44:47], 0
	s_waitcnt lgkmcnt(7)
	v_mfma_f32_16x16x32_bf16 v[4:7], v[168:171], v[36:39], 0
	s_waitcnt lgkmcnt(6)
	v_mfma_f32_16x16x32_bf16 v[12:15], v[172:175], v[40:43], v[12:15]
	s_waitcnt lgkmcnt(6)
	v_mfma_f32_16x16x32_bf16 v[4:7], v[172:175], v[32:35], v[4:7]
	s_nop 6
	v_cvt_pk_bf16_f32 v12, v12, v13
	v_cvt_pk_bf16_f32 v13, v14, v15
	v_cvt_pk_bf16_f32 v4, v4, v5
	v_cvt_pk_bf16_f32 v5, v6, v7
	v_lshl_add_u64 v[6:7], v[80:81], 0, v[0:1]
	global_store_dwordx2 v[2:3], v[12:13], off offset:2048
	global_store_dwordx2 v[6:7], v[4:5], off
	s_waitcnt lgkmcnt(5)
	v_mfma_f32_16x16x32_bf16 v[12:15], v[176:179], v[44:47], 0
	s_waitcnt lgkmcnt(5)
	v_mfma_f32_16x16x32_bf16 v[4:7], v[176:179], v[36:39], 0
	s_waitcnt lgkmcnt(4)
	v_mfma_f32_16x16x32_bf16 v[12:15], v[180:183], v[40:43], v[12:15]
	s_waitcnt lgkmcnt(4)
	v_mfma_f32_16x16x32_bf16 v[4:7], v[180:183], v[32:35], v[4:7]
	s_nop 6
	v_cvt_pk_bf16_f32 v12, v12, v13
	v_cvt_pk_bf16_f32 v13, v14, v15
	v_cvt_pk_bf16_f32 v4, v4, v5
	v_cvt_pk_bf16_f32 v5, v6, v7
	v_lshl_add_u64 v[6:7], v[82:83], 0, v[0:1]
	global_store_dwordx2 v[2:3], v[12:13], off offset:2560
	global_store_dwordx2 v[6:7], v[4:5], off
	s_waitcnt lgkmcnt(3)
	v_mfma_f32_16x16x32_bf16 v[12:15], v[184:187], v[44:47], 0
	s_waitcnt lgkmcnt(3)
	v_mfma_f32_16x16x32_bf16 v[4:7], v[184:187], v[36:39], 0
	s_waitcnt lgkmcnt(2)
	v_mfma_f32_16x16x32_bf16 v[12:15], v[188:191], v[40:43], v[12:15]
	s_waitcnt lgkmcnt(2)
	v_mfma_f32_16x16x32_bf16 v[4:7], v[188:191], v[32:35], v[4:7]
	s_nop 6
	v_cvt_pk_bf16_f32 v12, v12, v13
	v_cvt_pk_bf16_f32 v13, v14, v15
	v_cvt_pk_bf16_f32 v4, v4, v5
	v_cvt_pk_bf16_f32 v5, v6, v7
	v_lshl_add_u64 v[6:7], v[84:85], 0, v[0:1]
	global_store_dwordx2 v[2:3], v[12:13], off offset:3072
	global_store_dwordx2 v[6:7], v[4:5], off
	s_waitcnt lgkmcnt(1)
	v_mfma_f32_16x16x32_bf16 v[12:15], v[192:195], v[44:47], 0
	v_lshl_add_u64 v[0:1], v[86:87], 0, v[0:1]
	s_waitcnt lgkmcnt(0)
	v_mfma_f32_16x16x32_bf16 v[12:15], v[196:199], v[40:43], v[12:15]
	s_nop 7
	v_cvt_pk_bf16_f32 v12, v12, v13
	v_cvt_pk_bf16_f32 v13, v14, v15
	global_store_dwordx2 v[2:3], v[12:13], off offset:3584
	s_waitcnt lgkmcnt(1)
	v_mfma_f32_16x16x32_bf16 v[2:5], v[192:195], v[36:39], 0
	s_waitcnt lgkmcnt(0)
	v_mfma_f32_16x16x32_bf16 v[2:5], v[196:199], v[32:35], v[2:5]
	s_nop 7
	v_cvt_pk_bf16_f32 v2, v2, v3
	v_cvt_pk_bf16_f32 v3, v4, v5
	global_store_dwordx2 v[0:1], v[2:3], off
	s_cbranch_scc0 .LBB0_933
